# speedup vs baseline: 1.0165x; 1.0010x over previous
.Lup_loop:
	s_waitcnt lgkmcnt(0)
	v_mfma_f32_16x16x32_bf16 v[128:131], v[48:51], v[32:35], v[128:131]
	ds_read_b128 v[80:83], v13 offset:0
	v_mfma_f32_16x16x32_bf16 v[132:135], v[48:51], v[36:39], v[132:135]
	s_add_u32 m0, s20, 0x6000
	v_mfma_f32_16x16x32_bf16 v[136:139], v[48:51], v[40:43], v[136:139]
	ds_read_b128 v[84:87], v13 offset:2048
	v_mfma_f32_16x16x32_bf16 v[140:143], v[48:51], v[44:47], v[140:143]
	global_load_lds_dwordx4 v4, s[18:19]
	v_mfma_f32_16x16x32_bf16 v[144:147], v[52:55], v[32:35], v[144:147]
	ds_read_b128 v[88:91], v13 offset:4096
	v_mfma_f32_16x16x32_bf16 v[148:151], v[52:55], v[36:39], v[148:151]
	s_add_u32 m0, s20, 0x7000
	v_mfma_f32_16x16x32_bf16 v[152:155], v[52:55], v[40:43], v[152:155]
	ds_read_b128 v[92:95], v13 offset:6144
	v_mfma_f32_16x16x32_bf16 v[156:159], v[52:55], v[44:47], v[156:159]
	global_load_lds_dwordx4 v5, s[18:19]
	v_mfma_f32_16x16x32_bf16 v[160:163], v[56:59], v[32:35], v[160:163]
	ds_read_b128 v[96:99], v15 offset:0
	v_mfma_f32_16x16x32_bf16 v[164:167], v[56:59], v[36:39], v[164:167]
	s_add_u32 m0, s20, 0x8000
	v_mfma_f32_16x16x32_bf16 v[168:171], v[56:59], v[40:43], v[168:171]
	ds_read_b128 v[100:103], v15 offset:2048
	v_mfma_f32_16x16x32_bf16 v[172:175], v[56:59], v[44:47], v[172:175]
	global_load_lds_dwordx4 v6, s[18:19]
	v_mfma_f32_16x16x32_bf16 v[176:179], v[60:63], v[32:35], v[176:179]
	ds_read_b128 v[104:107], v15 offset:4096
	v_mfma_f32_16x16x32_bf16 v[180:183], v[60:63], v[36:39], v[180:183]
	s_add_u32 m0, s20, 0x9000
	v_mfma_f32_16x16x32_bf16 v[184:187], v[60:63], v[40:43], v[184:187]
	ds_read_b128 v[108:111], v15 offset:6144
	v_mfma_f32_16x16x32_bf16 v[188:191], v[60:63], v[44:47], v[188:191]
	global_load_lds_dwordx4 v7, s[18:19]
	v_mfma_f32_16x16x32_bf16 v[192:195], v[64:67], v[32:35], v[192:195]
	ds_read_b128 v[112:115], v15 offset:8192
	v_mfma_f32_16x16x32_bf16 v[196:199], v[64:67], v[36:39], v[196:199]
	s_add_u32 m0, s20, 0xa000
	v_mfma_f32_16x16x32_bf16 v[200:203], v[64:67], v[40:43], v[200:203]
	ds_read_b128 v[116:119], v15 offset:10240
	v_mfma_f32_16x16x32_bf16 v[204:207], v[64:67], v[44:47], v[204:207]
	global_load_lds_dwordx4 v8, s[18:19]
	v_mfma_f32_16x16x32_bf16 v[208:211], v[68:71], v[32:35], v[208:211]
	ds_read_b128 v[120:123], v15 offset:12288
	v_mfma_f32_16x16x32_bf16 v[212:215], v[68:71], v[36:39], v[212:215]
	s_add_u32 m0, s20, 0xb000
	v_mfma_f32_16x16x32_bf16 v[216:219], v[68:71], v[40:43], v[216:219]
	ds_read_b128 v[124:127], v15 offset:14336
	v_mfma_f32_16x16x32_bf16 v[220:223], v[68:71], v[44:47], v[220:223]
	global_load_lds_dwordx4 v9, s[18:19]
	v_mfma_f32_16x16x32_bf16 v[224:227], v[72:75], v[32:35], v[224:227]
	v_mfma_f32_16x16x32_bf16 v[228:231], v[72:75], v[36:39], v[228:231]
	v_mfma_f32_16x16x32_bf16 v[232:235], v[72:75], v[40:43], v[232:235]
	v_mfma_f32_16x16x32_bf16 v[236:239], v[72:75], v[44:47], v[236:239]
	v_mfma_f32_16x16x32_bf16 v[240:243], v[76:79], v[32:35], v[240:243]
	s_add_u32 s16, s16, 0x80
	s_addc_u32 s17, s17, 0
	s_add_u32 s18, s18, 0x80
	s_addc_u32 s19, s19, 0
	v_mfma_f32_16x16x32_bf16 v[244:247], v[76:79], v[36:39], v[244:247]
	s_add_u32 s20, s20, 0xc000
	s_sub_u32 s22, s20, 0x24000
	s_cmp_ge_u32 s20, 0x24000
	s_cselect_b32 s20, s22, s20
	v_mfma_f32_16x16x32_bf16 v[248:251], v[76:79], v[40:43], v[248:251]
	v_add_u32_e32 v12, s21, v10
	v_add_u32_e32 v14, s21, v11
	v_xor_b32_e32 v13, 64, v12
	v_xor_b32_e32 v15, 64, v14
	v_mfma_f32_16x16x32_bf16 v[252:255], v[76:79], v[44:47], v[252:255]
	s_add_u32 s21, s21, 0xc000
	s_sub_u32 s23, s21, 0x24000
	s_cmp_ge_u32 s21, 0x24000
	s_cselect_b32 s21, s23, s21
	s_waitcnt vmcnt(12) lgkmcnt(0)
	s_barrier
	v_mfma_f32_16x16x32_bf16 v[128:131], v[96:99], v[80:83], v[128:131]
	ds_read_b128 v[32:35], v12 offset:0
	v_mfma_f32_16x16x32_bf16 v[132:135], v[96:99], v[84:87], v[132:135]
	s_add_u32 m0, s20, 0x0
	v_mfma_f32_16x16x32_bf16 v[136:139], v[96:99], v[88:91], v[136:139]
	ds_read_b128 v[36:39], v12 offset:2048
	v_mfma_f32_16x16x32_bf16 v[140:143], v[96:99], v[92:95], v[140:143]
	global_load_lds_dwordx4 v2, s[16:17]
	v_mfma_f32_16x16x32_bf16 v[144:147], v[100:103], v[80:83], v[144:147]
	ds_read_b128 v[40:43], v12 offset:4096
	v_mfma_f32_16x16x32_bf16 v[148:151], v[100:103], v[84:87], v[148:151]
	s_add_u32 m0, s20, 0x1000
	v_mfma_f32_16x16x32_bf16 v[152:155], v[100:103], v[88:91], v[152:155]
	ds_read_b128 v[44:47], v12 offset:6144
	v_mfma_f32_16x16x32_bf16 v[156:159], v[100:103], v[92:95], v[156:159]
	global_load_lds_dwordx4 v3, s[16:17]
	v_mfma_f32_16x16x32_bf16 v[160:163], v[104:107], v[80:83], v[160:163]
	ds_read_b128 v[48:51], v14 offset:0
	v_mfma_f32_16x16x32_bf16 v[164:167], v[104:107], v[84:87], v[164:167]
	s_add_u32 m0, s20, 0x2000
	v_mfma_f32_16x16x32_bf16 v[168:171], v[104:107], v[88:91], v[168:171]
	ds_read_b128 v[52:55], v14 offset:2048
	v_mfma_f32_16x16x32_bf16 v[172:175], v[104:107], v[92:95], v[172:175]
	global_load_lds_dwordx4 v4, s[16:17]
	v_mfma_f32_16x16x32_bf16 v[176:179], v[108:111], v[80:83], v[176:179]
	ds_read_b128 v[56:59], v14 offset:4096
	v_mfma_f32_16x16x32_bf16 v[180:183], v[108:111], v[84:87], v[180:183]
	s_add_u32 m0, s20, 0x3000
	v_mfma_f32_16x16x32_bf16 v[184:187], v[108:111], v[88:91], v[184:187]
	ds_read_b128 v[60:63], v14 offset:6144
	v_mfma_f32_16x16x32_bf16 v[188:191], v[108:111], v[92:95], v[188:191]
	global_load_lds_dwordx4 v5, s[16:17]
	v_mfma_f32_16x16x32_bf16 v[192:195], v[112:115], v[80:83], v[192:195]
	ds_read_b128 v[64:67], v14 offset:8192
	v_mfma_f32_16x16x32_bf16 v[196:199], v[112:115], v[84:87], v[196:199]
	s_add_u32 m0, s20, 0x4000
	v_mfma_f32_16x16x32_bf16 v[200:203], v[112:115], v[88:91], v[200:203]
	ds_read_b128 v[68:71], v14 offset:10240
	v_mfma_f32_16x16x32_bf16 v[204:207], v[112:115], v[92:95], v[204:207]
	global_load_lds_dwordx4 v2, s[18:19]
	v_mfma_f32_16x16x32_bf16 v[208:211], v[116:119], v[80:83], v[208:211]
	ds_read_b128 v[72:75], v14 offset:12288
	v_mfma_f32_16x16x32_bf16 v[212:215], v[116:119], v[84:87], v[212:215]
	s_add_u32 m0, s20, 0x5000
	v_mfma_f32_16x16x32_bf16 v[216:219], v[116:119], v[88:91], v[216:219]
	ds_read_b128 v[76:79], v14 offset:14336
	v_mfma_f32_16x16x32_bf16 v[220:223], v[116:119], v[92:95], v[220:223]
	global_load_lds_dwordx4 v3, s[18:19]
	v_mfma_f32_16x16x32_bf16 v[224:227], v[120:123], v[80:83], v[224:227]
	v_mfma_f32_16x16x32_bf16 v[228:231], v[120:123], v[84:87], v[228:231]
	v_mfma_f32_16x16x32_bf16 v[232:235], v[120:123], v[88:91], v[232:235]
	v_mfma_f32_16x16x32_bf16 v[236:239], v[120:123], v[92:95], v[236:239]
	v_mfma_f32_16x16x32_bf16 v[240:243], v[124:127], v[80:83], v[240:243]
	v_mfma_f32_16x16x32_bf16 v[244:247], v[124:127], v[84:87], v[244:247]
	v_mfma_f32_16x16x32_bf16 v[248:251], v[124:127], v[88:91], v[248:251]
	v_mfma_f32_16x16x32_bf16 v[252:255], v[124:127], v[92:95], v[252:255]
	s_add_u32 s15, s15, 1
	s_cmp_lt_u32 s15, 9
	s_cbranch_scc1 .Lup_loop
	s_waitcnt lgkmcnt(0)
	v_mfma_f32_16x16x32_bf16 v[128:131], v[48:51], v[32:35], v[128:131]
	ds_read_b128 v[80:83], v13 offset:0
	v_mfma_f32_16x16x32_bf16 v[132:135], v[48:51], v[36:39], v[132:135]
	s_add_u32 m0, s20, 0x6000
	v_mfma_f32_16x16x32_bf16 v[136:139], v[48:51], v[40:43], v[136:139]
	ds_read_b128 v[84:87], v13 offset:2048
	v_mfma_f32_16x16x32_bf16 v[140:143], v[48:51], v[44:47], v[140:143]
	global_load_lds_dwordx4 v4, s[18:19]
	v_mfma_f32_16x16x32_bf16 v[144:147], v[52:55], v[32:35], v[144:147]
	ds_read_b128 v[88:91], v13 offset:4096
	v_mfma_f32_16x16x32_bf16 v[148:151], v[52:55], v[36:39], v[148:151]
	s_add_u32 m0, s20, 0x7000
	v_mfma_f32_16x16x32_bf16 v[152:155], v[52:55], v[40:43], v[152:155]
	ds_read_b128 v[92:95], v13 offset:6144
	v_mfma_f32_16x16x32_bf16 v[156:159], v[52:55], v[44:47], v[156:159]
	global_load_lds_dwordx4 v5, s[18:19]
	v_mfma_f32_16x16x32_bf16 v[160:163], v[56:59], v[32:35], v[160:163]
	ds_read_b128 v[96:99], v15 offset:0
	v_mfma_f32_16x16x32_bf16 v[164:167], v[56:59], v[36:39], v[164:167]
	s_add_u32 m0, s20, 0x8000
	v_mfma_f32_16x16x32_bf16 v[168:171], v[56:59], v[40:43], v[168:171]
	ds_read_b128 v[100:103], v15 offset:2048
	v_mfma_f32_16x16x32_bf16 v[172:175], v[56:59], v[44:47], v[172:175]
	global_load_lds_dwordx4 v6, s[18:19]
	v_mfma_f32_16x16x32_bf16 v[176:179], v[60:63], v[32:35], v[176:179]
	ds_read_b128 v[104:107], v15 offset:4096
	v_mfma_f32_16x16x32_bf16 v[180:183], v[60:63], v[36:39], v[180:183]
	s_add_u32 m0, s20, 0x9000
	v_mfma_f32_16x16x32_bf16 v[184:187], v[60:63], v[40:43], v[184:187]
	ds_read_b128 v[108:111], v15 offset:6144
	v_mfma_f32_16x16x32_bf16 v[188:191], v[60:63], v[44:47], v[188:191]
	global_load_lds_dwordx4 v7, s[18:19]
	v_mfma_f32_16x16x32_bf16 v[192:195], v[64:67], v[32:35], v[192:195]
	ds_read_b128 v[112:115], v15 offset:8192
	v_mfma_f32_16x16x32_bf16 v[196:199], v[64:67], v[36:39], v[196:199]
	s_add_u32 m0, s20, 0xa000
	v_mfma_f32_16x16x32_bf16 v[200:203], v[64:67], v[40:43], v[200:203]
	ds_read_b128 v[116:119], v15 offset:10240
	v_mfma_f32_16x16x32_bf16 v[204:207], v[64:67], v[44:47], v[204:207]
	global_load_lds_dwordx4 v8, s[18:19]
	v_mfma_f32_16x16x32_bf16 v[208:211], v[68:71], v[32:35], v[208:211]
	ds_read_b128 v[120:123], v15 offset:12288
	v_mfma_f32_16x16x32_bf16 v[212:215], v[68:71], v[36:39], v[212:215]
	s_add_u32 m0, s20, 0xb000
	v_mfma_f32_16x16x32_bf16 v[216:219], v[68:71], v[40:43], v[216:219]
	ds_read_b128 v[124:127], v15 offset:14336
	v_mfma_f32_16x16x32_bf16 v[220:223], v[68:71], v[44:47], v[220:223]
	global_load_lds_dwordx4 v9, s[18:19]
	v_mfma_f32_16x16x32_bf16 v[224:227], v[72:75], v[32:35], v[224:227]
	v_mfma_f32_16x16x32_bf16 v[228:231], v[72:75], v[36:39], v[228:231]
	v_mfma_f32_16x16x32_bf16 v[232:235], v[72:75], v[40:43], v[232:235]
	v_mfma_f32_16x16x32_bf16 v[236:239], v[72:75], v[44:47], v[236:239]
	v_mfma_f32_16x16x32_bf16 v[240:243], v[76:79], v[32:35], v[240:243]
	s_add_u32 s16, s16, 0x80
	s_addc_u32 s17, s17, 0
	s_add_u32 s18, s18, 0x80
	s_addc_u32 s19, s19, 0
	v_mfma_f32_16x16x32_bf16 v[244:247], v[76:79], v[36:39], v[244:247]
	s_add_u32 s20, s20, 0xc000
	s_sub_u32 s22, s20, 0x24000
	s_cmp_ge_u32 s20, 0x24000
	s_cselect_b32 s20, s22, s20
	v_mfma_f32_16x16x32_bf16 v[248:251], v[76:79], v[40:43], v[248:251]
	v_add_u32_e32 v12, s21, v10
	v_add_u32_e32 v14, s21, v11
	v_xor_b32_e32 v13, 64, v12
	v_xor_b32_e32 v15, 64, v14
	v_mfma_f32_16x16x32_bf16 v[252:255], v[76:79], v[44:47], v[252:255]
	s_add_u32 s21, s21, 0xc000
	s_sub_u32 s23, s21, 0x24000
	s_cmp_ge_u32 s21, 0x24000
	s_cselect_b32 s21, s23, s21
	s_waitcnt vmcnt(12) lgkmcnt(0)
	s_barrier
	v_mfma_f32_16x16x32_bf16 v[128:131], v[96:99], v[80:83], v[128:131]
	ds_read_b128 v[32:35], v12 offset:0
	v_mfma_f32_16x16x32_bf16 v[132:135], v[96:99], v[84:87], v[132:135]
	ds_read_b128 v[36:39], v12 offset:2048
	v_mfma_f32_16x16x32_bf16 v[136:139], v[96:99], v[88:91], v[136:139]
	ds_read_b128 v[40:43], v12 offset:4096
	v_mfma_f32_16x16x32_bf16 v[140:143], v[96:99], v[92:95], v[140:143]
	ds_read_b128 v[44:47], v12 offset:6144
	v_mfma_f32_16x16x32_bf16 v[144:147], v[100:103], v[80:83], v[144:147]
	ds_read_b128 v[48:51], v14 offset:0
	v_mfma_f32_16x16x32_bf16 v[148:151], v[100:103], v[84:87], v[148:151]
	ds_read_b128 v[52:55], v14 offset:2048
	v_mfma_f32_16x16x32_bf16 v[152:155], v[100:103], v[88:91], v[152:155]
	ds_read_b128 v[56:59], v14 offset:4096
	v_mfma_f32_16x16x32_bf16 v[156:159], v[100:103], v[92:95], v[156:159]
	ds_read_b128 v[60:63], v14 offset:6144
	v_mfma_f32_16x16x32_bf16 v[160:163], v[104:107], v[80:83], v[160:163]
	ds_read_b128 v[64:67], v14 offset:8192
	v_mfma_f32_16x16x32_bf16 v[164:167], v[104:107], v[84:87], v[164:167]
	ds_read_b128 v[68:71], v14 offset:10240
	v_mfma_f32_16x16x32_bf16 v[168:171], v[104:107], v[88:91], v[168:171]
	ds_read_b128 v[72:75], v14 offset:12288
	v_mfma_f32_16x16x32_bf16 v[172:175], v[104:107], v[92:95], v[172:175]
	ds_read_b128 v[76:79], v14 offset:14336
	v_mfma_f32_16x16x32_bf16 v[176:179], v[108:111], v[80:83], v[176:179]
	v_mfma_f32_16x16x32_bf16 v[180:183], v[108:111], v[84:87], v[180:183]
	v_mfma_f32_16x16x32_bf16 v[184:187], v[108:111], v[88:91], v[184:187]
	v_mfma_f32_16x16x32_bf16 v[188:191], v[108:111], v[92:95], v[188:191]
	v_mfma_f32_16x16x32_bf16 v[192:195], v[112:115], v[80:83], v[192:195]
	v_mfma_f32_16x16x32_bf16 v[196:199], v[112:115], v[84:87], v[196:199]
	v_mfma_f32_16x16x32_bf16 v[200:203], v[112:115], v[88:91], v[200:203]
	v_mfma_f32_16x16x32_bf16 v[204:207], v[112:115], v[92:95], v[204:207]
	v_mfma_f32_16x16x32_bf16 v[208:211], v[116:119], v[80:83], v[208:211]
	v_mfma_f32_16x16x32_bf16 v[212:215], v[116:119], v[84:87], v[212:215]
	v_mfma_f32_16x16x32_bf16 v[216:219], v[116:119], v[88:91], v[216:219]
	v_mfma_f32_16x16x32_bf16 v[220:223], v[116:119], v[92:95], v[220:223]
	v_mfma_f32_16x16x32_bf16 v[224:227], v[120:123], v[80:83], v[224:227]
	v_mfma_f32_16x16x32_bf16 v[228:231], v[120:123], v[84:87], v[228:231]
	v_mfma_f32_16x16x32_bf16 v[232:235], v[120:123], v[88:91], v[232:235]
	v_mfma_f32_16x16x32_bf16 v[236:239], v[120:123], v[92:95], v[236:239]
	v_mfma_f32_16x16x32_bf16 v[240:243], v[124:127], v[80:83], v[240:243]
	v_mfma_f32_16x16x32_bf16 v[244:247], v[124:127], v[84:87], v[244:247]
	v_mfma_f32_16x16x32_bf16 v[248:251], v[124:127], v[88:91], v[248:251]
	v_mfma_f32_16x16x32_bf16 v[252:255], v[124:127], v[92:95], v[252:255]
	s_waitcnt lgkmcnt(0)
	v_mfma_f32_16x16x32_bf16 v[128:131], v[48:51], v[32:35], v[128:131]
	ds_read_b128 v[80:83], v13 offset:0
	v_mfma_f32_16x16x32_bf16 v[132:135], v[48:51], v[36:39], v[132:135]
	ds_read_b128 v[84:87], v13 offset:2048
	v_mfma_f32_16x16x32_bf16 v[136:139], v[48:51], v[40:43], v[136:139]
	ds_read_b128 v[88:91], v13 offset:4096
	v_mfma_f32_16x16x32_bf16 v[140:143], v[48:51], v[44:47], v[140:143]
	ds_read_b128 v[92:95], v13 offset:6144
	v_mfma_f32_16x16x32_bf16 v[144:147], v[52:55], v[32:35], v[144:147]
	ds_read_b128 v[96:99], v15 offset:0
	v_mfma_f32_16x16x32_bf16 v[148:151], v[52:55], v[36:39], v[148:151]
	ds_read_b128 v[100:103], v15 offset:2048
	v_mfma_f32_16x16x32_bf16 v[152:155], v[52:55], v[40:43], v[152:155]
	ds_read_b128 v[104:107], v15 offset:4096
	v_mfma_f32_16x16x32_bf16 v[156:159], v[52:55], v[44:47], v[156:159]
	ds_read_b128 v[108:111], v15 offset:6144
	v_mfma_f32_16x16x32_bf16 v[160:163], v[56:59], v[32:35], v[160:163]
	ds_read_b128 v[112:115], v15 offset:8192
	v_mfma_f32_16x16x32_bf16 v[164:167], v[56:59], v[36:39], v[164:167]
	ds_read_b128 v[116:119], v15 offset:10240
	v_mfma_f32_16x16x32_bf16 v[168:171], v[56:59], v[40:43], v[168:171]
	ds_read_b128 v[120:123], v15 offset:12288
	v_mfma_f32_16x16x32_bf16 v[172:175], v[56:59], v[44:47], v[172:175]
	ds_read_b128 v[124:127], v15 offset:14336
	v_mfma_f32_16x16x32_bf16 v[176:179], v[60:63], v[32:35], v[176:179]
	v_mfma_f32_16x16x32_bf16 v[180:183], v[60:63], v[36:39], v[180:183]
	v_mfma_f32_16x16x32_bf16 v[184:187], v[60:63], v[40:43], v[184:187]
	v_mfma_f32_16x16x32_bf16 v[188:191], v[60:63], v[44:47], v[188:191]
	v_mfma_f32_16x16x32_bf16 v[192:195], v[64:67], v[32:35], v[192:195]
	v_mfma_f32_16x16x32_bf16 v[196:199], v[64:67], v[36:39], v[196:199]
	v_mfma_f32_16x16x32_bf16 v[200:203], v[64:67], v[40:43], v[200:203]
	v_mfma_f32_16x16x32_bf16 v[204:207], v[64:67], v[44:47], v[204:207]
	v_mfma_f32_16x16x32_bf16 v[208:211], v[68:71], v[32:35], v[208:211]
	v_mfma_f32_16x16x32_bf16 v[212:215], v[68:71], v[36:39], v[212:215]
	v_mfma_f32_16x16x32_bf16 v[216:219], v[68:71], v[40:43], v[216:219]
	v_mfma_f32_16x16x32_bf16 v[220:223], v[68:71], v[44:47], v[220:223]
	v_mfma_f32_16x16x32_bf16 v[224:227], v[72:75], v[32:35], v[224:227]
	v_mfma_f32_16x16x32_bf16 v[228:231], v[72:75], v[36:39], v[228:231]
	v_mfma_f32_16x16x32_bf16 v[232:235], v[72:75], v[40:43], v[232:235]
	v_mfma_f32_16x16x32_bf16 v[236:239], v[72:75], v[44:47], v[236:239]
	v_mfma_f32_16x16x32_bf16 v[240:243], v[76:79], v[32:35], v[240:243]
	v_add_u32_e32 v12, s21, v10
	v_add_u32_e32 v14, s21, v11
	v_xor_b32_e32 v13, 64, v12
	v_xor_b32_e32 v15, 64, v14
	v_mfma_f32_16x16x32_bf16 v[244:247], v[76:79], v[36:39], v[244:247]
	s_add_u32 s21, s21, 0xc000
	s_sub_u32 s23, s21, 0x24000
	s_cmp_ge_u32 s21, 0x24000
	s_cselect_b32 s21, s23, s21
	v_mfma_f32_16x16x32_bf16 v[248:251], v[76:79], v[40:43], v[248:251]
	v_mfma_f32_16x16x32_bf16 v[252:255], v[76:79], v[44:47], v[252:255]
	s_waitcnt vmcnt(0) lgkmcnt(0)
	s_barrier
	v_mfma_f32_16x16x32_bf16 v[128:131], v[96:99], v[80:83], v[128:131]
	ds_read_b128 v[32:35], v12 offset:0
	v_mfma_f32_16x16x32_bf16 v[132:135], v[96:99], v[84:87], v[132:135]
	ds_read_b128 v[36:39], v12 offset:2048
	v_mfma_f32_16x16x32_bf16 v[136:139], v[96:99], v[88:91], v[136:139]
	ds_read_b128 v[40:43], v12 offset:4096
	v_mfma_f32_16x16x32_bf16 v[140:143], v[96:99], v[92:95], v[140:143]
	ds_read_b128 v[44:47], v12 offset:6144
	v_mfma_f32_16x16x32_bf16 v[144:147], v[100:103], v[80:83], v[144:147]
	ds_read_b128 v[48:51], v14 offset:0
	v_mfma_f32_16x16x32_bf16 v[148:151], v[100:103], v[84:87], v[148:151]
	ds_read_b128 v[52:55], v14 offset:2048
	v_mfma_f32_16x16x32_bf16 v[152:155], v[100:103], v[88:91], v[152:155]
	ds_read_b128 v[56:59], v14 offset:4096
	v_mfma_f32_16x16x32_bf16 v[156:159], v[100:103], v[92:95], v[156:159]
	ds_read_b128 v[60:63], v14 offset:6144
	v_mfma_f32_16x16x32_bf16 v[160:163], v[104:107], v[80:83], v[160:163]
	ds_read_b128 v[64:67], v14 offset:8192
	v_mfma_f32_16x16x32_bf16 v[164:167], v[104:107], v[84:87], v[164:167]
	ds_read_b128 v[68:71], v14 offset:10240
	v_mfma_f32_16x16x32_bf16 v[168:171], v[104:107], v[88:91], v[168:171]
	ds_read_b128 v[72:75], v14 offset:12288
	v_mfma_f32_16x16x32_bf16 v[172:175], v[104:107], v[92:95], v[172:175]
	ds_read_b128 v[76:79], v14 offset:14336
	v_mfma_f32_16x16x32_bf16 v[176:179], v[108:111], v[80:83], v[176:179]
	v_mfma_f32_16x16x32_bf16 v[180:183], v[108:111], v[84:87], v[180:183]
	v_mfma_f32_16x16x32_bf16 v[184:187], v[108:111], v[88:91], v[184:187]
	v_mfma_f32_16x16x32_bf16 v[188:191], v[108:111], v[92:95], v[188:191]
	v_mfma_f32_16x16x32_bf16 v[192:195], v[112:115], v[80:83], v[192:195]
	v_mfma_f32_16x16x32_bf16 v[196:199], v[112:115], v[84:87], v[196:199]
	v_mfma_f32_16x16x32_bf16 v[200:203], v[112:115], v[88:91], v[200:203]
	v_mfma_f32_16x16x32_bf16 v[204:207], v[112:115], v[92:95], v[204:207]
	v_mfma_f32_16x16x32_bf16 v[208:211], v[116:119], v[80:83], v[208:211]
	v_mfma_f32_16x16x32_bf16 v[212:215], v[116:119], v[84:87], v[212:215]
	v_mfma_f32_16x16x32_bf16 v[216:219], v[116:119], v[88:91], v[216:219]
	v_mfma_f32_16x16x32_bf16 v[220:223], v[116:119], v[92:95], v[220:223]
	v_mfma_f32_16x16x32_bf16 v[224:227], v[120:123], v[80:83], v[224:227]
	v_mfma_f32_16x16x32_bf16 v[228:231], v[120:123], v[84:87], v[228:231]
	v_mfma_f32_16x16x32_bf16 v[232:235], v[120:123], v[88:91], v[232:235]
	v_mfma_f32_16x16x32_bf16 v[236:239], v[120:123], v[92:95], v[236:239]
	v_mfma_f32_16x16x32_bf16 v[240:243], v[124:127], v[80:83], v[240:243]
	v_mfma_f32_16x16x32_bf16 v[244:247], v[124:127], v[84:87], v[244:247]
	v_mfma_f32_16x16x32_bf16 v[248:251], v[124:127], v[88:91], v[248:251]
	v_mfma_f32_16x16x32_bf16 v[252:255], v[124:127], v[92:95], v[252:255]
	s_waitcnt lgkmcnt(0)
	v_mfma_f32_16x16x32_bf16 v[128:131], v[48:51], v[32:35], v[128:131]
	ds_read_b128 v[80:83], v13 offset:0
	v_mfma_f32_16x16x32_bf16 v[132:135], v[48:51], v[36:39], v[132:135]
	ds_read_b128 v[84:87], v13 offset:2048
	v_mfma_f32_16x16x32_bf16 v[136:139], v[48:51], v[40:43], v[136:139]
	ds_read_b128 v[88:91], v13 offset:4096
	v_mfma_f32_16x16x32_bf16 v[140:143], v[48:51], v[44:47], v[140:143]
	ds_read_b128 v[92:95], v13 offset:6144
	v_mfma_f32_16x16x32_bf16 v[144:147], v[52:55], v[32:35], v[144:147]
	ds_read_b128 v[96:99], v15 offset:0
	v_mfma_f32_16x16x32_bf16 v[148:151], v[52:55], v[36:39], v[148:151]
	ds_read_b128 v[100:103], v15 offset:2048
	v_mfma_f32_16x16x32_bf16 v[152:155], v[52:55], v[40:43], v[152:155]
	ds_read_b128 v[104:107], v15 offset:4096
	v_mfma_f32_16x16x32_bf16 v[156:159], v[52:55], v[44:47], v[156:159]
	ds_read_b128 v[108:111], v15 offset:6144
	v_mfma_f32_16x16x32_bf16 v[160:163], v[56:59], v[32:35], v[160:163]
	ds_read_b128 v[112:115], v15 offset:8192
	v_mfma_f32_16x16x32_bf16 v[164:167], v[56:59], v[36:39], v[164:167]
	ds_read_b128 v[116:119], v15 offset:10240
	v_mfma_f32_16x16x32_bf16 v[168:171], v[56:59], v[40:43], v[168:171]
	ds_read_b128 v[120:123], v15 offset:12288
	v_mfma_f32_16x16x32_bf16 v[172:175], v[56:59], v[44:47], v[172:175]
	ds_read_b128 v[124:127], v15 offset:14336
	v_mfma_f32_16x16x32_bf16 v[176:179], v[60:63], v[32:35], v[176:179]
	v_mfma_f32_16x16x32_bf16 v[180:183], v[60:63], v[36:39], v[180:183]
	v_mfma_f32_16x16x32_bf16 v[184:187], v[60:63], v[40:43], v[184:187]
	v_mfma_f32_16x16x32_bf16 v[188:191], v[60:63], v[44:47], v[188:191]
	v_mfma_f32_16x16x32_bf16 v[192:195], v[64:67], v[32:35], v[192:195]
	v_mfma_f32_16x16x32_bf16 v[196:199], v[64:67], v[36:39], v[196:199]
	v_mfma_f32_16x16x32_bf16 v[200:203], v[64:67], v[40:43], v[200:203]
	v_mfma_f32_16x16x32_bf16 v[204:207], v[64:67], v[44:47], v[204:207]
	v_mfma_f32_16x16x32_bf16 v[208:211], v[68:71], v[32:35], v[208:211]
	v_mfma_f32_16x16x32_bf16 v[212:215], v[68:71], v[36:39], v[212:215]
	v_mfma_f32_16x16x32_bf16 v[216:219], v[68:71], v[40:43], v[216:219]
	v_mfma_f32_16x16x32_bf16 v[220:223], v[68:71], v[44:47], v[220:223]
	v_mfma_f32_16x16x32_bf16 v[224:227], v[72:75], v[32:35], v[224:227]
	v_mfma_f32_16x16x32_bf16 v[228:231], v[72:75], v[36:39], v[228:231]
	v_mfma_f32_16x16x32_bf16 v[232:235], v[72:75], v[40:43], v[232:235]
	v_mfma_f32_16x16x32_bf16 v[236:239], v[72:75], v[44:47], v[236:239]
	v_mfma_f32_16x16x32_bf16 v[240:243], v[76:79], v[32:35], v[240:243]
	v_mfma_f32_16x16x32_bf16 v[244:247], v[76:79], v[36:39], v[244:247]
	v_mfma_f32_16x16x32_bf16 v[248:251], v[76:79], v[40:43], v[248:251]
	v_mfma_f32_16x16x32_bf16 v[252:255], v[76:79], v[44:47], v[252:255]
	s_waitcnt lgkmcnt(0)
	v_mfma_f32_16x16x32_bf16 v[128:131], v[96:99], v[80:83], v[128:131]
	v_mfma_f32_16x16x32_bf16 v[132:135], v[96:99], v[84:87], v[132:135]
	global_load_dwordx4 v[32:35], v21, s[8:9] offset:0
	v_mfma_f32_16x16x32_bf16 v[136:139], v[96:99], v[88:91], v[136:139]
	v_mfma_f32_16x16x32_bf16 v[140:143], v[96:99], v[92:95], v[140:143]
	global_load_dwordx4 v[36:39], v21, s[8:9] offset:16
	v_mfma_f32_16x16x32_bf16 v[144:147], v[100:103], v[80:83], v[144:147]
	v_mfma_f32_16x16x32_bf16 v[148:151], v[100:103], v[84:87], v[148:151]
	global_load_dwordx4 v[40:43], v21, s[8:9] offset:32
	v_mfma_f32_16x16x32_bf16 v[152:155], v[100:103], v[88:91], v[152:155]
	v_mfma_f32_16x16x32_bf16 v[156:159], v[100:103], v[92:95], v[156:159]
	global_load_dwordx4 v[44:47], v21, s[8:9] offset:48
	v_mfma_f32_16x16x32_bf16 v[160:163], v[104:107], v[80:83], v[160:163]
	v_mfma_f32_16x16x32_bf16 v[164:167], v[104:107], v[84:87], v[164:167]
	global_load_dwordx4 v[48:51], v21, s[8:9] offset:1024
	v_mfma_f32_16x16x32_bf16 v[168:171], v[104:107], v[88:91], v[168:171]
	v_mfma_f32_16x16x32_bf16 v[172:175], v[104:107], v[92:95], v[172:175]
	global_load_dwordx4 v[52:55], v21, s[8:9] offset:1040
	v_mfma_f32_16x16x32_bf16 v[176:179], v[108:111], v[80:83], v[176:179]
	v_mfma_f32_16x16x32_bf16 v[180:183], v[108:111], v[84:87], v[180:183]
	global_load_dwordx4 v[56:59], v21, s[8:9] offset:1056
	v_mfma_f32_16x16x32_bf16 v[184:187], v[108:111], v[88:91], v[184:187]
	v_mfma_f32_16x16x32_bf16 v[188:191], v[108:111], v[92:95], v[188:191]
	global_load_dwordx4 v[60:63], v21, s[8:9] offset:1072
	v_mfma_f32_16x16x32_bf16 v[192:195], v[112:115], v[80:83], v[192:195]
	v_mfma_f32_16x16x32_bf16 v[196:199], v[112:115], v[84:87], v[196:199]
	global_load_dwordx4 v[64:67], v21, s[8:9] offset:2048
	v_mfma_f32_16x16x32_bf16 v[200:203], v[112:115], v[88:91], v[200:203]
	v_mfma_f32_16x16x32_bf16 v[204:207], v[112:115], v[92:95], v[204:207]
	global_load_dwordx4 v[68:71], v21, s[8:9] offset:2064
	v_mfma_f32_16x16x32_bf16 v[208:211], v[116:119], v[80:83], v[208:211]
	v_mfma_f32_16x16x32_bf16 v[212:215], v[116:119], v[84:87], v[212:215]
	global_load_dwordx4 v[72:75], v21, s[8:9] offset:2080
	v_mfma_f32_16x16x32_bf16 v[216:219], v[116:119], v[88:91], v[216:219]
	v_mfma_f32_16x16x32_bf16 v[220:223], v[116:119], v[92:95], v[220:223]
	global_load_dwordx4 v[76:79], v21, s[8:9] offset:2096
	v_mfma_f32_16x16x32_bf16 v[224:227], v[120:123], v[80:83], v[224:227]
	v_mfma_f32_16x16x32_bf16 v[228:231], v[120:123], v[84:87], v[228:231]
	v_mfma_f32_16x16x32_bf16 v[232:235], v[120:123], v[88:91], v[232:235]
	v_mfma_f32_16x16x32_bf16 v[236:239], v[120:123], v[92:95], v[236:239]
	v_mfma_f32_16x16x32_bf16 v[240:243], v[124:127], v[80:83], v[240:243]
	v_mfma_f32_16x16x32_bf16 v[244:247], v[124:127], v[84:87], v[244:247]
	v_mfma_f32_16x16x32_bf16 v[248:251], v[124:127], v[88:91], v[248:251]
	v_mfma_f32_16x16x32_bf16 v[252:255], v[124:127], v[92:95], v[252:255]
	global_load_dwordx4 v[80:83], v21, s[8:9] offset:3072
	global_load_dwordx4 v[84:87], v21, s[8:9] offset:3088
	global_load_dwordx4 v[88:91], v21, s[8:9] offset:3104
	global_load_dwordx4 v[92:95], v21, s[8:9] offset:3120
	v_mov_b32_e32 v31, 0x358637bd
	s_waitcnt vmcnt(0)
	v_add_f32_e32 v32, v32, v33
	v_add_f32_e32 v34, v34, v35
	v_add_f32_e32 v36, v36, v37
	v_add_f32_e32 v38, v38, v39
	v_add_f32_e32 v40, v40, v41
	v_add_f32_e32 v42, v42, v43
	v_add_f32_e32 v44, v44, v45
	v_add_f32_e32 v46, v46, v47
	v_add_f32_e32 v32, v32, v34
	v_add_f32_e32 v36, v36, v38
	v_add_f32_e32 v40, v40, v42
	v_add_f32_e32 v44, v44, v46
	v_add_f32_e32 v32, v32, v36
	v_add_f32_e32 v40, v40, v44
	s_nop 0
	v_add_f32_e32 v32, v32, v40
	v_add_f32_e32 v48, v48, v49
	v_add_f32_e32 v50, v50, v51
	v_add_f32_e32 v52, v52, v53
	v_add_f32_e32 v54, v54, v55
	v_add_f32_e32 v56, v56, v57
	v_add_f32_e32 v58, v58, v59
	v_add_f32_e32 v60, v60, v61
	v_add_f32_e32 v62, v62, v63
	v_add_f32_e32 v48, v48, v50
	v_add_f32_e32 v52, v52, v54
	v_add_f32_e32 v56, v56, v58
	v_add_f32_e32 v60, v60, v62
	v_add_f32_e32 v48, v48, v52
	v_add_f32_e32 v56, v56, v60
	s_nop 0
	v_add_f32_e32 v48, v48, v56
	v_add_f32_e32 v64, v64, v65
	v_add_f32_e32 v66, v66, v67
	v_add_f32_e32 v68, v68, v69
	v_add_f32_e32 v70, v70, v71
	v_add_f32_e32 v72, v72, v73
	v_add_f32_e32 v74, v74, v75
	v_add_f32_e32 v76, v76, v77
	v_add_f32_e32 v78, v78, v79
	v_add_f32_e32 v64, v64, v66
	v_add_f32_e32 v68, v68, v70
	v_add_f32_e32 v72, v72, v74
	v_add_f32_e32 v76, v76, v78
	v_add_f32_e32 v64, v64, v68
	v_add_f32_e32 v72, v72, v76
	s_nop 0
	v_add_f32_e32 v64, v64, v72
	v_add_f32_e32 v80, v80, v81
	v_add_f32_e32 v82, v82, v83
	v_add_f32_e32 v84, v84, v85
	v_add_f32_e32 v86, v86, v87
	v_add_f32_e32 v88, v88, v89
	v_add_f32_e32 v90, v90, v91
	v_add_f32_e32 v92, v92, v93
	v_add_f32_e32 v94, v94, v95
	v_add_f32_e32 v80, v80, v82
	v_add_f32_e32 v84, v84, v86
	v_add_f32_e32 v88, v88, v90
	v_add_f32_e32 v92, v92, v94
	v_add_f32_e32 v80, v80, v84
	v_add_f32_e32 v88, v88, v92
	s_nop 0
	v_add_f32_e32 v80, v80, v88
	v_fmamk_f32 v20, v32, 0x3aaaaaab, v31
	v_fmamk_f32 v22, v48, 0x3aaaaaab, v31
	v_fmamk_f32 v24, v64, 0x3aaaaaab, v31
	v_fmamk_f32 v26, v80, 0x3aaaaaab, v31
	v_rsq_f32_e32 v20, v20
	v_rsq_f32_e32 v22, v22
	v_rsq_f32_e32 v24, v24
	v_rsq_f32_e32 v26, v26
	s_nop 0
	v_pk_mul_f32 v[128:129], v[128:129], v[20:21] op_sel_hi:[1,0]
	v_pk_mul_f32 v[130:131], v[130:131], v[20:21] op_sel_hi:[1,0]
	v_pk_mul_f32 v[144:145], v[144:145], v[20:21] op_sel_hi:[1,0]
	v_pk_mul_f32 v[146:147], v[146:147], v[20:21] op_sel_hi:[1,0]
	v_pk_mul_f32 v[32:33], v[128:129], s[26:27]
	v_pk_mul_f32 v[34:35], v[130:131], s[26:27]
	v_pk_mul_f32 v[36:37], v[144:145], s[26:27]
	v_pk_mul_f32 v[38:39], v[146:147], s[26:27]
	v_pk_fma_f32 v[32:33], v[128:129], v[32:33], s[28:29] neg_lo:[1,0,0] neg_hi:[1,0,0]
	v_pk_fma_f32 v[34:35], v[130:131], v[34:35], s[28:29] neg_lo:[1,0,0] neg_hi:[1,0,0]
	v_pk_fma_f32 v[36:37], v[144:145], v[36:37], s[28:29] neg_lo:[1,0,0] neg_hi:[1,0,0]
	v_pk_fma_f32 v[38:39], v[146:147], v[38:39], s[28:29] neg_lo:[1,0,0] neg_hi:[1,0,0]
	v_pk_mul_f32 v[32:33], v[128:129], v[32:33]
	v_pk_mul_f32 v[34:35], v[130:131], v[34:35]
	v_pk_mul_f32 v[36:37], v[144:145], v[36:37]
	v_pk_mul_f32 v[38:39], v[146:147], v[38:39]
	v_exp_f32_e32 v32, v32
	v_pk_mul_f32 v[160:161], v[160:161], v[20:21] op_sel_hi:[1,0]
	v_pk_mul_f32 v[162:163], v[162:163], v[20:21] op_sel_hi:[1,0]
	v_exp_f32_e32 v33, v33
	v_pk_mul_f32 v[176:177], v[176:177], v[20:21] op_sel_hi:[1,0]
	v_pk_mul_f32 v[178:179], v[178:179], v[20:21] op_sel_hi:[1,0]
	v_exp_f32_e32 v34, v34
	v_pk_mul_f32 v[40:41], v[160:161], s[26:27]
	v_pk_mul_f32 v[42:43], v[162:163], s[26:27]
	v_exp_f32_e32 v35, v35
	v_pk_mul_f32 v[44:45], v[176:177], s[26:27]
	v_pk_mul_f32 v[46:47], v[178:179], s[26:27]
	v_exp_f32_e32 v36, v36
	v_pk_fma_f32 v[40:41], v[160:161], v[40:41], s[28:29] neg_lo:[1,0,0] neg_hi:[1,0,0]
	v_pk_fma_f32 v[42:43], v[162:163], v[42:43], s[28:29] neg_lo:[1,0,0] neg_hi:[1,0,0]
	v_exp_f32_e32 v37, v37
	v_pk_fma_f32 v[44:45], v[176:177], v[44:45], s[28:29] neg_lo:[1,0,0] neg_hi:[1,0,0]
	v_pk_fma_f32 v[46:47], v[178:179], v[46:47], s[28:29] neg_lo:[1,0,0] neg_hi:[1,0,0]
	v_exp_f32_e32 v38, v38
	v_pk_mul_f32 v[40:41], v[160:161], v[40:41]
	v_pk_mul_f32 v[42:43], v[162:163], v[42:43]
	v_exp_f32_e32 v39, v39
	v_pk_mul_f32 v[44:45], v[176:177], v[44:45]
	v_pk_mul_f32 v[46:47], v[178:179], v[46:47]
	v_pk_add_f32 v[32:33], v[32:33], s[30:31]
	v_pk_add_f32 v[34:35], v[34:35], s[30:31]
	v_pk_add_f32 v[36:37], v[36:37], s[30:31]
	v_pk_add_f32 v[38:39], v[38:39], s[30:31]
	v_rcp_f32_e32 v32, v32
	v_rcp_f32_e32 v33, v33
	v_rcp_f32_e32 v34, v34
	v_rcp_f32_e32 v35, v35
	v_rcp_f32_e32 v36, v36
	v_rcp_f32_e32 v37, v37
	v_rcp_f32_e32 v38, v38
	v_rcp_f32_e32 v39, v39
	v_exp_f32_e32 v40, v40
	v_pk_mul_f32 v[192:193], v[192:193], v[20:21] op_sel_hi:[1,0]
	v_pk_mul_f32 v[194:195], v[194:195], v[20:21] op_sel_hi:[1,0]
	v_exp_f32_e32 v41, v41
	v_pk_mul_f32 v[208:209], v[208:209], v[20:21] op_sel_hi:[1,0]
	v_pk_mul_f32 v[210:211], v[210:211], v[20:21] op_sel_hi:[1,0]
	v_exp_f32_e32 v42, v42
	v_pk_mul_f32 v[48:49], v[192:193], s[26:27]
	v_pk_mul_f32 v[50:51], v[194:195], s[26:27]
	v_exp_f32_e32 v43, v43
	v_pk_mul_f32 v[52:53], v[208:209], s[26:27]
	v_pk_mul_f32 v[54:55], v[210:211], s[26:27]
	v_exp_f32_e32 v44, v44
	v_pk_fma_f32 v[48:49], v[192:193], v[48:49], s[28:29] neg_lo:[1,0,0] neg_hi:[1,0,0]
	v_pk_fma_f32 v[50:51], v[194:195], v[50:51], s[28:29] neg_lo:[1,0,0] neg_hi:[1,0,0]
	v_exp_f32_e32 v45, v45
	v_pk_fma_f32 v[52:53], v[208:209], v[52:53], s[28:29] neg_lo:[1,0,0] neg_hi:[1,0,0]
	v_pk_fma_f32 v[54:55], v[210:211], v[54:55], s[28:29] neg_lo:[1,0,0] neg_hi:[1,0,0]
	v_exp_f32_e32 v46, v46
	v_pk_mul_f32 v[48:49], v[192:193], v[48:49]
	v_pk_mul_f32 v[50:51], v[194:195], v[50:51]
	v_exp_f32_e32 v47, v47
	v_pk_mul_f32 v[52:53], v[208:209], v[52:53]
	v_pk_mul_f32 v[54:55], v[210:211], v[54:55]
	v_pk_add_f32 v[40:41], v[40:41], s[30:31]
	v_pk_add_f32 v[42:43], v[42:43], s[30:31]
	v_pk_add_f32 v[44:45], v[44:45], s[30:31]
	v_pk_add_f32 v[46:47], v[46:47], s[30:31]
	v_rcp_f32_e32 v40, v40
	v_pk_mul_f32 v[128:129], v[128:129], v[32:33]
	v_pk_mul_f32 v[130:131], v[130:131], v[34:35]
	v_rcp_f32_e32 v41, v41
	v_pk_mul_f32 v[144:145], v[144:145], v[36:37]
	v_pk_mul_f32 v[146:147], v[146:147], v[38:39]
	v_rcp_f32_e32 v42, v42
	v_cvt_pk_bf16_f32 v64, v128, v129
	v_cvt_pk_bf16_f32 v65, v130, v131
	v_rcp_f32_e32 v43, v43
	v_cvt_pk_bf16_f32 v66, v144, v145
	v_cvt_pk_bf16_f32 v67, v146, v147
	v_rcp_f32_e32 v44, v44
	global_store_dwordx2 v16, v[64:65], s[10:11]
	global_store_dwordx2 v16, v[66:67], s[10:11] offset:32
	v_rcp_f32_e32 v45, v45
	v_rcp_f32_e32 v46, v46
	v_rcp_f32_e32 v47, v47
	v_exp_f32_e32 v48, v48
	v_pk_mul_f32 v[224:225], v[224:225], v[20:21] op_sel_hi:[1,0]
	v_pk_mul_f32 v[226:227], v[226:227], v[20:21] op_sel_hi:[1,0]
	v_exp_f32_e32 v49, v49
	v_pk_mul_f32 v[240:241], v[240:241], v[20:21] op_sel_hi:[1,0]
	v_pk_mul_f32 v[242:243], v[242:243], v[20:21] op_sel_hi:[1,0]
	v_exp_f32_e32 v50, v50
	v_pk_mul_f32 v[32:33], v[224:225], s[26:27]
	v_pk_mul_f32 v[34:35], v[226:227], s[26:27]
	v_exp_f32_e32 v51, v51
	v_pk_mul_f32 v[36:37], v[240:241], s[26:27]
	v_pk_mul_f32 v[38:39], v[242:243], s[26:27]
	v_exp_f32_e32 v52, v52
	v_pk_fma_f32 v[32:33], v[224:225], v[32:33], s[28:29] neg_lo:[1,0,0] neg_hi:[1,0,0]
	v_pk_fma_f32 v[34:35], v[226:227], v[34:35], s[28:29] neg_lo:[1,0,0] neg_hi:[1,0,0]
	v_exp_f32_e32 v53, v53
	v_pk_fma_f32 v[36:37], v[240:241], v[36:37], s[28:29] neg_lo:[1,0,0] neg_hi:[1,0,0]
	v_pk_fma_f32 v[38:39], v[242:243], v[38:39], s[28:29] neg_lo:[1,0,0] neg_hi:[1,0,0]
	v_exp_f32_e32 v54, v54
	v_pk_mul_f32 v[32:33], v[224:225], v[32:33]
	v_pk_mul_f32 v[34:35], v[226:227], v[34:35]
	v_exp_f32_e32 v55, v55
	v_pk_mul_f32 v[36:37], v[240:241], v[36:37]
	v_pk_mul_f32 v[38:39], v[242:243], v[38:39]
	v_pk_add_f32 v[48:49], v[48:49], s[30:31]
	v_pk_add_f32 v[50:51], v[50:51], s[30:31]
	v_pk_add_f32 v[52:53], v[52:53], s[30:31]
	v_pk_add_f32 v[54:55], v[54:55], s[30:31]
	v_rcp_f32_e32 v48, v48
	v_pk_mul_f32 v[160:161], v[160:161], v[40:41]
	v_pk_mul_f32 v[162:163], v[162:163], v[42:43]
	v_rcp_f32_e32 v49, v49
	v_pk_mul_f32 v[176:177], v[176:177], v[44:45]
	v_pk_mul_f32 v[178:179], v[178:179], v[46:47]
	v_rcp_f32_e32 v50, v50
	v_cvt_pk_bf16_f32 v68, v160, v161
	v_cvt_pk_bf16_f32 v69, v162, v163
	v_rcp_f32_e32 v51, v51
	v_cvt_pk_bf16_f32 v70, v176, v177
	v_cvt_pk_bf16_f32 v71, v178, v179
	v_rcp_f32_e32 v52, v52
	global_store_dwordx2 v16, v[68:69], s[10:11] offset:64
	global_store_dwordx2 v16, v[70:71], s[10:11] offset:96
	v_rcp_f32_e32 v53, v53
	v_rcp_f32_e32 v54, v54
	v_rcp_f32_e32 v55, v55
	v_exp_f32_e32 v32, v32
	v_pk_mul_f32 v[132:133], v[132:133], v[22:23] op_sel_hi:[1,0]
	v_pk_mul_f32 v[134:135], v[134:135], v[22:23] op_sel_hi:[1,0]
	v_exp_f32_e32 v33, v33
	v_pk_mul_f32 v[148:149], v[148:149], v[22:23] op_sel_hi:[1,0]
	v_pk_mul_f32 v[150:151], v[150:151], v[22:23] op_sel_hi:[1,0]
	v_exp_f32_e32 v34, v34
	v_pk_mul_f32 v[40:41], v[132:133], s[26:27]
	v_pk_mul_f32 v[42:43], v[134:135], s[26:27]
	v_exp_f32_e32 v35, v35
	v_pk_mul_f32 v[44:45], v[148:149], s[26:27]
	v_pk_mul_f32 v[46:47], v[150:151], s[26:27]
	v_exp_f32_e32 v36, v36
	v_pk_fma_f32 v[40:41], v[132:133], v[40:41], s[28:29] neg_lo:[1,0,0] neg_hi:[1,0,0]
	v_pk_fma_f32 v[42:43], v[134:135], v[42:43], s[28:29] neg_lo:[1,0,0] neg_hi:[1,0,0]
	v_exp_f32_e32 v37, v37
	v_pk_fma_f32 v[44:45], v[148:149], v[44:45], s[28:29] neg_lo:[1,0,0] neg_hi:[1,0,0]
	v_pk_fma_f32 v[46:47], v[150:151], v[46:47], s[28:29] neg_lo:[1,0,0] neg_hi:[1,0,0]
	v_exp_f32_e32 v38, v38
	v_pk_mul_f32 v[40:41], v[132:133], v[40:41]
	v_pk_mul_f32 v[42:43], v[134:135], v[42:43]
	v_exp_f32_e32 v39, v39
	v_pk_mul_f32 v[44:45], v[148:149], v[44:45]
	v_pk_mul_f32 v[46:47], v[150:151], v[46:47]
	v_pk_add_f32 v[32:33], v[32:33], s[30:31]
	v_pk_add_f32 v[34:35], v[34:35], s[30:31]
	v_pk_add_f32 v[36:37], v[36:37], s[30:31]
	v_pk_add_f32 v[38:39], v[38:39], s[30:31]
	v_rcp_f32_e32 v32, v32
	v_pk_mul_f32 v[192:193], v[192:193], v[48:49]
	v_pk_mul_f32 v[194:195], v[194:195], v[50:51]
	v_rcp_f32_e32 v33, v33
	v_pk_mul_f32 v[208:209], v[208:209], v[52:53]
	v_pk_mul_f32 v[210:211], v[210:211], v[54:55]
	v_rcp_f32_e32 v34, v34
	v_cvt_pk_bf16_f32 v64, v192, v193
	v_cvt_pk_bf16_f32 v65, v194, v195
	v_rcp_f32_e32 v35, v35
	v_cvt_pk_bf16_f32 v66, v208, v209
	v_cvt_pk_bf16_f32 v67, v210, v211
	v_rcp_f32_e32 v36, v36
	global_store_dwordx2 v16, v[64:65], s[10:11] offset:128
	global_store_dwordx2 v16, v[66:67], s[10:11] offset:160
	v_rcp_f32_e32 v37, v37
	v_rcp_f32_e32 v38, v38
	v_rcp_f32_e32 v39, v39
	v_exp_f32_e32 v40, v40
	v_pk_mul_f32 v[164:165], v[164:165], v[22:23] op_sel_hi:[1,0]
	v_pk_mul_f32 v[166:167], v[166:167], v[22:23] op_sel_hi:[1,0]
	v_exp_f32_e32 v41, v41
	v_pk_mul_f32 v[180:181], v[180:181], v[22:23] op_sel_hi:[1,0]
	v_pk_mul_f32 v[182:183], v[182:183], v[22:23] op_sel_hi:[1,0]
	v_exp_f32_e32 v42, v42
	v_pk_mul_f32 v[48:49], v[164:165], s[26:27]
	v_pk_mul_f32 v[50:51], v[166:167], s[26:27]
	v_exp_f32_e32 v43, v43
	v_pk_mul_f32 v[52:53], v[180:181], s[26:27]
	v_pk_mul_f32 v[54:55], v[182:183], s[26:27]
	v_exp_f32_e32 v44, v44
	v_pk_fma_f32 v[48:49], v[164:165], v[48:49], s[28:29] neg_lo:[1,0,0] neg_hi:[1,0,0]
	v_pk_fma_f32 v[50:51], v[166:167], v[50:51], s[28:29] neg_lo:[1,0,0] neg_hi:[1,0,0]
	v_exp_f32_e32 v45, v45
	v_pk_fma_f32 v[52:53], v[180:181], v[52:53], s[28:29] neg_lo:[1,0,0] neg_hi:[1,0,0]
	v_pk_fma_f32 v[54:55], v[182:183], v[54:55], s[28:29] neg_lo:[1,0,0] neg_hi:[1,0,0]
	v_exp_f32_e32 v46, v46
	v_pk_mul_f32 v[48:49], v[164:165], v[48:49]
	v_pk_mul_f32 v[50:51], v[166:167], v[50:51]
	v_exp_f32_e32 v47, v47
	v_pk_mul_f32 v[52:53], v[180:181], v[52:53]
	v_pk_mul_f32 v[54:55], v[182:183], v[54:55]
	v_pk_add_f32 v[40:41], v[40:41], s[30:31]
	v_pk_add_f32 v[42:43], v[42:43], s[30:31]
	v_pk_add_f32 v[44:45], v[44:45], s[30:31]
	v_pk_add_f32 v[46:47], v[46:47], s[30:31]
	v_rcp_f32_e32 v40, v40
	v_pk_mul_f32 v[224:225], v[224:225], v[32:33]
	v_pk_mul_f32 v[226:227], v[226:227], v[34:35]
	v_rcp_f32_e32 v41, v41
	v_pk_mul_f32 v[240:241], v[240:241], v[36:37]
	v_pk_mul_f32 v[242:243], v[242:243], v[38:39]
	v_rcp_f32_e32 v42, v42
	v_cvt_pk_bf16_f32 v68, v224, v225
	v_cvt_pk_bf16_f32 v69, v226, v227
	v_rcp_f32_e32 v43, v43
	v_cvt_pk_bf16_f32 v70, v240, v241
	v_cvt_pk_bf16_f32 v71, v242, v243
	v_rcp_f32_e32 v44, v44
	global_store_dwordx2 v16, v[68:69], s[10:11] offset:192
	global_store_dwordx2 v16, v[70:71], s[10:11] offset:224
	v_rcp_f32_e32 v45, v45
	v_rcp_f32_e32 v46, v46
	v_rcp_f32_e32 v47, v47
	v_exp_f32_e32 v48, v48
	v_pk_mul_f32 v[196:197], v[196:197], v[22:23] op_sel_hi:[1,0]
	v_pk_mul_f32 v[198:199], v[198:199], v[22:23] op_sel_hi:[1,0]
	v_exp_f32_e32 v49, v49
	v_pk_mul_f32 v[212:213], v[212:213], v[22:23] op_sel_hi:[1,0]
	v_pk_mul_f32 v[214:215], v[214:215], v[22:23] op_sel_hi:[1,0]
	v_exp_f32_e32 v50, v50
	v_pk_mul_f32 v[32:33], v[196:197], s[26:27]
	v_pk_mul_f32 v[34:35], v[198:199], s[26:27]
	v_exp_f32_e32 v51, v51
	v_pk_mul_f32 v[36:37], v[212:213], s[26:27]
	v_pk_mul_f32 v[38:39], v[214:215], s[26:27]
	v_exp_f32_e32 v52, v52
	v_pk_fma_f32 v[32:33], v[196:197], v[32:33], s[28:29] neg_lo:[1,0,0] neg_hi:[1,0,0]
	v_pk_fma_f32 v[34:35], v[198:199], v[34:35], s[28:29] neg_lo:[1,0,0] neg_hi:[1,0,0]
	v_exp_f32_e32 v53, v53
	v_pk_fma_f32 v[36:37], v[212:213], v[36:37], s[28:29] neg_lo:[1,0,0] neg_hi:[1,0,0]
	v_pk_fma_f32 v[38:39], v[214:215], v[38:39], s[28:29] neg_lo:[1,0,0] neg_hi:[1,0,0]
	v_exp_f32_e32 v54, v54
	v_pk_mul_f32 v[32:33], v[196:197], v[32:33]
	v_pk_mul_f32 v[34:35], v[198:199], v[34:35]
	v_exp_f32_e32 v55, v55
	v_pk_mul_f32 v[36:37], v[212:213], v[36:37]
	v_pk_mul_f32 v[38:39], v[214:215], v[38:39]
	v_pk_add_f32 v[48:49], v[48:49], s[30:31]
	v_pk_add_f32 v[50:51], v[50:51], s[30:31]
	v_pk_add_f32 v[52:53], v[52:53], s[30:31]
	v_pk_add_f32 v[54:55], v[54:55], s[30:31]
	v_rcp_f32_e32 v48, v48
	v_pk_mul_f32 v[132:133], v[132:133], v[40:41]
	v_pk_mul_f32 v[134:135], v[134:135], v[42:43]
	v_rcp_f32_e32 v49, v49
	v_pk_mul_f32 v[148:149], v[148:149], v[44:45]
	v_pk_mul_f32 v[150:151], v[150:151], v[46:47]
	v_rcp_f32_e32 v50, v50
	v_cvt_pk_bf16_f32 v64, v132, v133
	v_cvt_pk_bf16_f32 v65, v134, v135
	v_rcp_f32_e32 v51, v51
	v_cvt_pk_bf16_f32 v66, v148, v149
	v_cvt_pk_bf16_f32 v67, v150, v151
	v_rcp_f32_e32 v52, v52
	global_store_dwordx2 v17, v[64:65], s[10:11]
	global_store_dwordx2 v17, v[66:67], s[10:11] offset:32
	v_rcp_f32_e32 v53, v53
	v_rcp_f32_e32 v54, v54
	v_rcp_f32_e32 v55, v55
	v_exp_f32_e32 v32, v32
	v_pk_mul_f32 v[228:229], v[228:229], v[22:23] op_sel_hi:[1,0]
	v_pk_mul_f32 v[230:231], v[230:231], v[22:23] op_sel_hi:[1,0]
	v_exp_f32_e32 v33, v33
	v_pk_mul_f32 v[244:245], v[244:245], v[22:23] op_sel_hi:[1,0]
	v_pk_mul_f32 v[246:247], v[246:247], v[22:23] op_sel_hi:[1,0]
	v_exp_f32_e32 v34, v34
	v_pk_mul_f32 v[40:41], v[228:229], s[26:27]
	v_pk_mul_f32 v[42:43], v[230:231], s[26:27]
	v_exp_f32_e32 v35, v35
	v_pk_mul_f32 v[44:45], v[244:245], s[26:27]
	v_pk_mul_f32 v[46:47], v[246:247], s[26:27]
	v_exp_f32_e32 v36, v36
	v_pk_fma_f32 v[40:41], v[228:229], v[40:41], s[28:29] neg_lo:[1,0,0] neg_hi:[1,0,0]
	v_pk_fma_f32 v[42:43], v[230:231], v[42:43], s[28:29] neg_lo:[1,0,0] neg_hi:[1,0,0]
	v_exp_f32_e32 v37, v37
	v_pk_fma_f32 v[44:45], v[244:245], v[44:45], s[28:29] neg_lo:[1,0,0] neg_hi:[1,0,0]
	v_pk_fma_f32 v[46:47], v[246:247], v[46:47], s[28:29] neg_lo:[1,0,0] neg_hi:[1,0,0]
	v_exp_f32_e32 v38, v38
	v_pk_mul_f32 v[40:41], v[228:229], v[40:41]
	v_pk_mul_f32 v[42:43], v[230:231], v[42:43]
	v_exp_f32_e32 v39, v39
	v_pk_mul_f32 v[44:45], v[244:245], v[44:45]
	v_pk_mul_f32 v[46:47], v[246:247], v[46:47]
	v_pk_add_f32 v[32:33], v[32:33], s[30:31]
	v_pk_add_f32 v[34:35], v[34:35], s[30:31]
	v_pk_add_f32 v[36:37], v[36:37], s[30:31]
	v_pk_add_f32 v[38:39], v[38:39], s[30:31]
	v_rcp_f32_e32 v32, v32
	v_pk_mul_f32 v[164:165], v[164:165], v[48:49]
	v_pk_mul_f32 v[166:167], v[166:167], v[50:51]
	v_rcp_f32_e32 v33, v33
	v_pk_mul_f32 v[180:181], v[180:181], v[52:53]
	v_pk_mul_f32 v[182:183], v[182:183], v[54:55]
	v_rcp_f32_e32 v34, v34
	v_cvt_pk_bf16_f32 v68, v164, v165
	v_cvt_pk_bf16_f32 v69, v166, v167
	v_rcp_f32_e32 v35, v35
	v_cvt_pk_bf16_f32 v70, v180, v181
	v_cvt_pk_bf16_f32 v71, v182, v183
	v_rcp_f32_e32 v36, v36
	global_store_dwordx2 v17, v[68:69], s[10:11] offset:64
	global_store_dwordx2 v17, v[70:71], s[10:11] offset:96
	v_rcp_f32_e32 v37, v37
	v_rcp_f32_e32 v38, v38
	v_rcp_f32_e32 v39, v39
	v_exp_f32_e32 v40, v40
	v_pk_mul_f32 v[136:137], v[136:137], v[24:25] op_sel_hi:[1,0]
	v_pk_mul_f32 v[138:139], v[138:139], v[24:25] op_sel_hi:[1,0]
	v_exp_f32_e32 v41, v41
	v_pk_mul_f32 v[152:153], v[152:153], v[24:25] op_sel_hi:[1,0]
	v_pk_mul_f32 v[154:155], v[154:155], v[24:25] op_sel_hi:[1,0]
	v_exp_f32_e32 v42, v42
	v_pk_mul_f32 v[48:49], v[136:137], s[26:27]
	v_pk_mul_f32 v[50:51], v[138:139], s[26:27]
	v_exp_f32_e32 v43, v43
	v_pk_mul_f32 v[52:53], v[152:153], s[26:27]
	v_pk_mul_f32 v[54:55], v[154:155], s[26:27]
	v_exp_f32_e32 v44, v44
	v_pk_fma_f32 v[48:49], v[136:137], v[48:49], s[28:29] neg_lo:[1,0,0] neg_hi:[1,0,0]
	v_pk_fma_f32 v[50:51], v[138:139], v[50:51], s[28:29] neg_lo:[1,0,0] neg_hi:[1,0,0]
	v_exp_f32_e32 v45, v45
	v_pk_fma_f32 v[52:53], v[152:153], v[52:53], s[28:29] neg_lo:[1,0,0] neg_hi:[1,0,0]
	v_pk_fma_f32 v[54:55], v[154:155], v[54:55], s[28:29] neg_lo:[1,0,0] neg_hi:[1,0,0]
	v_exp_f32_e32 v46, v46
	v_pk_mul_f32 v[48:49], v[136:137], v[48:49]
	v_pk_mul_f32 v[50:51], v[138:139], v[50:51]
	v_exp_f32_e32 v47, v47
	v_pk_mul_f32 v[52:53], v[152:153], v[52:53]
	v_pk_mul_f32 v[54:55], v[154:155], v[54:55]
	v_pk_add_f32 v[40:41], v[40:41], s[30:31]
	v_pk_add_f32 v[42:43], v[42:43], s[30:31]
	v_pk_add_f32 v[44:45], v[44:45], s[30:31]
	v_pk_add_f32 v[46:47], v[46:47], s[30:31]
	v_rcp_f32_e32 v40, v40
	v_pk_mul_f32 v[196:197], v[196:197], v[32:33]
	v_pk_mul_f32 v[198:199], v[198:199], v[34:35]
	v_rcp_f32_e32 v41, v41
	v_pk_mul_f32 v[212:213], v[212:213], v[36:37]
	v_pk_mul_f32 v[214:215], v[214:215], v[38:39]
	v_rcp_f32_e32 v42, v42
	v_cvt_pk_bf16_f32 v64, v196, v197
	v_cvt_pk_bf16_f32 v65, v198, v199
	v_rcp_f32_e32 v43, v43
	v_cvt_pk_bf16_f32 v66, v212, v213
	v_cvt_pk_bf16_f32 v67, v214, v215
	v_rcp_f32_e32 v44, v44
	global_store_dwordx2 v17, v[64:65], s[10:11] offset:128
	global_store_dwordx2 v17, v[66:67], s[10:11] offset:160
	v_rcp_f32_e32 v45, v45
	v_rcp_f32_e32 v46, v46
	v_rcp_f32_e32 v47, v47
	v_exp_f32_e32 v48, v48
	v_pk_mul_f32 v[168:169], v[168:169], v[24:25] op_sel_hi:[1,0]
	v_pk_mul_f32 v[170:171], v[170:171], v[24:25] op_sel_hi:[1,0]
	v_exp_f32_e32 v49, v49
	v_pk_mul_f32 v[184:185], v[184:185], v[24:25] op_sel_hi:[1,0]
	v_pk_mul_f32 v[186:187], v[186:187], v[24:25] op_sel_hi:[1,0]
	v_exp_f32_e32 v50, v50
	v_pk_mul_f32 v[32:33], v[168:169], s[26:27]
	v_pk_mul_f32 v[34:35], v[170:171], s[26:27]
	v_exp_f32_e32 v51, v51
	v_pk_mul_f32 v[36:37], v[184:185], s[26:27]
	v_pk_mul_f32 v[38:39], v[186:187], s[26:27]
	v_exp_f32_e32 v52, v52
	v_pk_fma_f32 v[32:33], v[168:169], v[32:33], s[28:29] neg_lo:[1,0,0] neg_hi:[1,0,0]
	v_pk_fma_f32 v[34:35], v[170:171], v[34:35], s[28:29] neg_lo:[1,0,0] neg_hi:[1,0,0]
	v_exp_f32_e32 v53, v53
	v_pk_fma_f32 v[36:37], v[184:185], v[36:37], s[28:29] neg_lo:[1,0,0] neg_hi:[1,0,0]
	v_pk_fma_f32 v[38:39], v[186:187], v[38:39], s[28:29] neg_lo:[1,0,0] neg_hi:[1,0,0]
	v_exp_f32_e32 v54, v54
	v_pk_mul_f32 v[32:33], v[168:169], v[32:33]
	v_pk_mul_f32 v[34:35], v[170:171], v[34:35]
	v_exp_f32_e32 v55, v55
	v_pk_mul_f32 v[36:37], v[184:185], v[36:37]
	v_pk_mul_f32 v[38:39], v[186:187], v[38:39]
	v_pk_add_f32 v[48:49], v[48:49], s[30:31]
	v_pk_add_f32 v[50:51], v[50:51], s[30:31]
	v_pk_add_f32 v[52:53], v[52:53], s[30:31]
	v_pk_add_f32 v[54:55], v[54:55], s[30:31]
	v_rcp_f32_e32 v48, v48
	v_pk_mul_f32 v[228:229], v[228:229], v[40:41]
	v_pk_mul_f32 v[230:231], v[230:231], v[42:43]
	v_rcp_f32_e32 v49, v49
	v_pk_mul_f32 v[244:245], v[244:245], v[44:45]
	v_pk_mul_f32 v[246:247], v[246:247], v[46:47]
	v_rcp_f32_e32 v50, v50
	v_cvt_pk_bf16_f32 v68, v228, v229
	v_cvt_pk_bf16_f32 v69, v230, v231
	v_rcp_f32_e32 v51, v51
	v_cvt_pk_bf16_f32 v70, v244, v245
	v_cvt_pk_bf16_f32 v71, v246, v247
	v_rcp_f32_e32 v52, v52
	global_store_dwordx2 v17, v[68:69], s[10:11] offset:192
	global_store_dwordx2 v17, v[70:71], s[10:11] offset:224
	v_rcp_f32_e32 v53, v53
	v_rcp_f32_e32 v54, v54
	v_rcp_f32_e32 v55, v55
	v_exp_f32_e32 v32, v32
	v_pk_mul_f32 v[200:201], v[200:201], v[24:25] op_sel_hi:[1,0]
	v_pk_mul_f32 v[202:203], v[202:203], v[24:25] op_sel_hi:[1,0]
	v_exp_f32_e32 v33, v33
	v_pk_mul_f32 v[216:217], v[216:217], v[24:25] op_sel_hi:[1,0]
	v_pk_mul_f32 v[218:219], v[218:219], v[24:25] op_sel_hi:[1,0]
	v_exp_f32_e32 v34, v34
	v_pk_mul_f32 v[40:41], v[200:201], s[26:27]
	v_pk_mul_f32 v[42:43], v[202:203], s[26:27]
	v_exp_f32_e32 v35, v35
	v_pk_mul_f32 v[44:45], v[216:217], s[26:27]
	v_pk_mul_f32 v[46:47], v[218:219], s[26:27]
	v_exp_f32_e32 v36, v36
	v_pk_fma_f32 v[40:41], v[200:201], v[40:41], s[28:29] neg_lo:[1,0,0] neg_hi:[1,0,0]
	v_pk_fma_f32 v[42:43], v[202:203], v[42:43], s[28:29] neg_lo:[1,0,0] neg_hi:[1,0,0]
	v_exp_f32_e32 v37, v37
	v_pk_fma_f32 v[44:45], v[216:217], v[44:45], s[28:29] neg_lo:[1,0,0] neg_hi:[1,0,0]
	v_pk_fma_f32 v[46:47], v[218:219], v[46:47], s[28:29] neg_lo:[1,0,0] neg_hi:[1,0,0]
	v_exp_f32_e32 v38, v38
	v_pk_mul_f32 v[40:41], v[200:201], v[40:41]
	v_pk_mul_f32 v[42:43], v[202:203], v[42:43]
	v_exp_f32_e32 v39, v39
	v_pk_mul_f32 v[44:45], v[216:217], v[44:45]
	v_pk_mul_f32 v[46:47], v[218:219], v[46:47]
	v_pk_add_f32 v[32:33], v[32:33], s[30:31]
	v_pk_add_f32 v[34:35], v[34:35], s[30:31]
	v_pk_add_f32 v[36:37], v[36:37], s[30:31]
	v_pk_add_f32 v[38:39], v[38:39], s[30:31]
	v_rcp_f32_e32 v32, v32
	v_pk_mul_f32 v[136:137], v[136:137], v[48:49]
	v_pk_mul_f32 v[138:139], v[138:139], v[50:51]
	v_rcp_f32_e32 v33, v33
	v_pk_mul_f32 v[152:153], v[152:153], v[52:53]
	v_pk_mul_f32 v[154:155], v[154:155], v[54:55]
	v_rcp_f32_e32 v34, v34
	v_cvt_pk_bf16_f32 v64, v136, v137
	v_cvt_pk_bf16_f32 v65, v138, v139
	v_rcp_f32_e32 v35, v35
	v_cvt_pk_bf16_f32 v66, v152, v153
	v_cvt_pk_bf16_f32 v67, v154, v155
	v_rcp_f32_e32 v36, v36
	global_store_dwordx2 v18, v[64:65], s[10:11]
	global_store_dwordx2 v18, v[66:67], s[10:11] offset:32
	v_rcp_f32_e32 v37, v37
	v_rcp_f32_e32 v38, v38
	v_rcp_f32_e32 v39, v39
	v_exp_f32_e32 v40, v40
	v_pk_mul_f32 v[232:233], v[232:233], v[24:25] op_sel_hi:[1,0]
	v_pk_mul_f32 v[234:235], v[234:235], v[24:25] op_sel_hi:[1,0]
	v_exp_f32_e32 v41, v41
	v_pk_mul_f32 v[248:249], v[248:249], v[24:25] op_sel_hi:[1,0]
	v_pk_mul_f32 v[250:251], v[250:251], v[24:25] op_sel_hi:[1,0]
	v_exp_f32_e32 v42, v42
	v_pk_mul_f32 v[48:49], v[232:233], s[26:27]
	v_pk_mul_f32 v[50:51], v[234:235], s[26:27]
	v_exp_f32_e32 v43, v43
	v_pk_mul_f32 v[52:53], v[248:249], s[26:27]
	v_pk_mul_f32 v[54:55], v[250:251], s[26:27]
	v_exp_f32_e32 v44, v44
	v_pk_fma_f32 v[48:49], v[232:233], v[48:49], s[28:29] neg_lo:[1,0,0] neg_hi:[1,0,0]
	v_pk_fma_f32 v[50:51], v[234:235], v[50:51], s[28:29] neg_lo:[1,0,0] neg_hi:[1,0,0]
	v_exp_f32_e32 v45, v45
	v_pk_fma_f32 v[52:53], v[248:249], v[52:53], s[28:29] neg_lo:[1,0,0] neg_hi:[1,0,0]
	v_pk_fma_f32 v[54:55], v[250:251], v[54:55], s[28:29] neg_lo:[1,0,0] neg_hi:[1,0,0]
	v_exp_f32_e32 v46, v46
	v_pk_mul_f32 v[48:49], v[232:233], v[48:49]
	v_pk_mul_f32 v[50:51], v[234:235], v[50:51]
	v_exp_f32_e32 v47, v47
	v_pk_mul_f32 v[52:53], v[248:249], v[52:53]
	v_pk_mul_f32 v[54:55], v[250:251], v[54:55]
	v_pk_add_f32 v[40:41], v[40:41], s[30:31]
	v_pk_add_f32 v[42:43], v[42:43], s[30:31]
	v_pk_add_f32 v[44:45], v[44:45], s[30:31]
	v_pk_add_f32 v[46:47], v[46:47], s[30:31]
	v_rcp_f32_e32 v40, v40
	v_pk_mul_f32 v[168:169], v[168:169], v[32:33]
	v_pk_mul_f32 v[170:171], v[170:171], v[34:35]
	v_rcp_f32_e32 v41, v41
	v_pk_mul_f32 v[184:185], v[184:185], v[36:37]
	v_pk_mul_f32 v[186:187], v[186:187], v[38:39]
	v_rcp_f32_e32 v42, v42
	v_cvt_pk_bf16_f32 v68, v168, v169
	v_cvt_pk_bf16_f32 v69, v170, v171
	v_rcp_f32_e32 v43, v43
	v_cvt_pk_bf16_f32 v70, v184, v185
	v_cvt_pk_bf16_f32 v71, v186, v187
	v_rcp_f32_e32 v44, v44
	global_store_dwordx2 v18, v[68:69], s[10:11] offset:64
	global_store_dwordx2 v18, v[70:71], s[10:11] offset:96
	v_rcp_f32_e32 v45, v45
	v_rcp_f32_e32 v46, v46
	v_rcp_f32_e32 v47, v47
	v_exp_f32_e32 v48, v48
	v_pk_mul_f32 v[140:141], v[140:141], v[26:27] op_sel_hi:[1,0]
	v_pk_mul_f32 v[142:143], v[142:143], v[26:27] op_sel_hi:[1,0]
	v_exp_f32_e32 v49, v49
	v_pk_mul_f32 v[156:157], v[156:157], v[26:27] op_sel_hi:[1,0]
	v_pk_mul_f32 v[158:159], v[158:159], v[26:27] op_sel_hi:[1,0]
	v_exp_f32_e32 v50, v50
	v_pk_mul_f32 v[32:33], v[140:141], s[26:27]
	v_pk_mul_f32 v[34:35], v[142:143], s[26:27]
	v_exp_f32_e32 v51, v51
	v_pk_mul_f32 v[36:37], v[156:157], s[26:27]
	v_pk_mul_f32 v[38:39], v[158:159], s[26:27]
	v_exp_f32_e32 v52, v52
	v_pk_fma_f32 v[32:33], v[140:141], v[32:33], s[28:29] neg_lo:[1,0,0] neg_hi:[1,0,0]
	v_pk_fma_f32 v[34:35], v[142:143], v[34:35], s[28:29] neg_lo:[1,0,0] neg_hi:[1,0,0]
	v_exp_f32_e32 v53, v53
	v_pk_fma_f32 v[36:37], v[156:157], v[36:37], s[28:29] neg_lo:[1,0,0] neg_hi:[1,0,0]
	v_pk_fma_f32 v[38:39], v[158:159], v[38:39], s[28:29] neg_lo:[1,0,0] neg_hi:[1,0,0]
	v_exp_f32_e32 v54, v54
	v_pk_mul_f32 v[32:33], v[140:141], v[32:33]
	v_pk_mul_f32 v[34:35], v[142:143], v[34:35]
	v_exp_f32_e32 v55, v55
	v_pk_mul_f32 v[36:37], v[156:157], v[36:37]
	v_pk_mul_f32 v[38:39], v[158:159], v[38:39]
	v_pk_add_f32 v[48:49], v[48:49], s[30:31]
	v_pk_add_f32 v[50:51], v[50:51], s[30:31]
	v_pk_add_f32 v[52:53], v[52:53], s[30:31]
	v_pk_add_f32 v[54:55], v[54:55], s[30:31]
	v_rcp_f32_e32 v48, v48
	v_pk_mul_f32 v[200:201], v[200:201], v[40:41]
	v_pk_mul_f32 v[202:203], v[202:203], v[42:43]
	v_rcp_f32_e32 v49, v49
	v_pk_mul_f32 v[216:217], v[216:217], v[44:45]
	v_pk_mul_f32 v[218:219], v[218:219], v[46:47]
	v_rcp_f32_e32 v50, v50
	v_cvt_pk_bf16_f32 v64, v200, v201
	v_cvt_pk_bf16_f32 v65, v202, v203
	v_rcp_f32_e32 v51, v51
	v_cvt_pk_bf16_f32 v66, v216, v217
	v_cvt_pk_bf16_f32 v67, v218, v219
	v_rcp_f32_e32 v52, v52
	global_store_dwordx2 v18, v[64:65], s[10:11] offset:128
	global_store_dwordx2 v18, v[66:67], s[10:11] offset:160
	v_rcp_f32_e32 v53, v53
	v_rcp_f32_e32 v54, v54
	v_rcp_f32_e32 v55, v55
	v_exp_f32_e32 v32, v32
	v_pk_mul_f32 v[172:173], v[172:173], v[26:27] op_sel_hi:[1,0]
	v_pk_mul_f32 v[174:175], v[174:175], v[26:27] op_sel_hi:[1,0]
	v_exp_f32_e32 v33, v33
	v_pk_mul_f32 v[188:189], v[188:189], v[26:27] op_sel_hi:[1,0]
	v_pk_mul_f32 v[190:191], v[190:191], v[26:27] op_sel_hi:[1,0]
	v_exp_f32_e32 v34, v34
	v_pk_mul_f32 v[40:41], v[172:173], s[26:27]
	v_pk_mul_f32 v[42:43], v[174:175], s[26:27]
	v_exp_f32_e32 v35, v35
	v_pk_mul_f32 v[44:45], v[188:189], s[26:27]
	v_pk_mul_f32 v[46:47], v[190:191], s[26:27]
	v_exp_f32_e32 v36, v36
	v_pk_fma_f32 v[40:41], v[172:173], v[40:41], s[28:29] neg_lo:[1,0,0] neg_hi:[1,0,0]
	v_pk_fma_f32 v[42:43], v[174:175], v[42:43], s[28:29] neg_lo:[1,0,0] neg_hi:[1,0,0]
	v_exp_f32_e32 v37, v37
	v_pk_fma_f32 v[44:45], v[188:189], v[44:45], s[28:29] neg_lo:[1,0,0] neg_hi:[1,0,0]
	v_pk_fma_f32 v[46:47], v[190:191], v[46:47], s[28:29] neg_lo:[1,0,0] neg_hi:[1,0,0]
	v_exp_f32_e32 v38, v38
	v_pk_mul_f32 v[40:41], v[172:173], v[40:41]
	v_pk_mul_f32 v[42:43], v[174:175], v[42:43]
	v_exp_f32_e32 v39, v39
	v_pk_mul_f32 v[44:45], v[188:189], v[44:45]
	v_pk_mul_f32 v[46:47], v[190:191], v[46:47]
	v_pk_add_f32 v[32:33], v[32:33], s[30:31]
	v_pk_add_f32 v[34:35], v[34:35], s[30:31]
	v_pk_add_f32 v[36:37], v[36:37], s[30:31]
	v_pk_add_f32 v[38:39], v[38:39], s[30:31]
	v_rcp_f32_e32 v32, v32
	v_pk_mul_f32 v[232:233], v[232:233], v[48:49]
	v_pk_mul_f32 v[234:235], v[234:235], v[50:51]
	v_rcp_f32_e32 v33, v33
	v_pk_mul_f32 v[248:249], v[248:249], v[52:53]
	v_pk_mul_f32 v[250:251], v[250:251], v[54:55]
	v_rcp_f32_e32 v34, v34
	v_cvt_pk_bf16_f32 v68, v232, v233
	v_cvt_pk_bf16_f32 v69, v234, v235
	v_rcp_f32_e32 v35, v35
	v_cvt_pk_bf16_f32 v70, v248, v249
	v_cvt_pk_bf16_f32 v71, v250, v251
	v_rcp_f32_e32 v36, v36
	global_store_dwordx2 v18, v[68:69], s[10:11] offset:192
	global_store_dwordx2 v18, v[70:71], s[10:11] offset:224
	v_rcp_f32_e32 v37, v37
	v_rcp_f32_e32 v38, v38
	v_rcp_f32_e32 v39, v39
	v_exp_f32_e32 v40, v40
	v_pk_mul_f32 v[204:205], v[204:205], v[26:27] op_sel_hi:[1,0]
	v_pk_mul_f32 v[206:207], v[206:207], v[26:27] op_sel_hi:[1,0]
	v_exp_f32_e32 v41, v41
	v_pk_mul_f32 v[220:221], v[220:221], v[26:27] op_sel_hi:[1,0]
	v_pk_mul_f32 v[222:223], v[222:223], v[26:27] op_sel_hi:[1,0]
	v_exp_f32_e32 v42, v42
	v_pk_mul_f32 v[48:49], v[204:205], s[26:27]
	v_pk_mul_f32 v[50:51], v[206:207], s[26:27]
	v_exp_f32_e32 v43, v43
	v_pk_mul_f32 v[52:53], v[220:221], s[26:27]
	v_pk_mul_f32 v[54:55], v[222:223], s[26:27]
	v_exp_f32_e32 v44, v44
	v_pk_fma_f32 v[48:49], v[204:205], v[48:49], s[28:29] neg_lo:[1,0,0] neg_hi:[1,0,0]
	v_pk_fma_f32 v[50:51], v[206:207], v[50:51], s[28:29] neg_lo:[1,0,0] neg_hi:[1,0,0]
	v_exp_f32_e32 v45, v45
	v_pk_fma_f32 v[52:53], v[220:221], v[52:53], s[28:29] neg_lo:[1,0,0] neg_hi:[1,0,0]
	v_pk_fma_f32 v[54:55], v[222:223], v[54:55], s[28:29] neg_lo:[1,0,0] neg_hi:[1,0,0]
	v_exp_f32_e32 v46, v46
	v_pk_mul_f32 v[48:49], v[204:205], v[48:49]
	v_pk_mul_f32 v[50:51], v[206:207], v[50:51]
	v_exp_f32_e32 v47, v47
	v_pk_mul_f32 v[52:53], v[220:221], v[52:53]
	v_pk_mul_f32 v[54:55], v[222:223], v[54:55]
	v_pk_add_f32 v[40:41], v[40:41], s[30:31]
	v_pk_add_f32 v[42:43], v[42:43], s[30:31]
	v_pk_add_f32 v[44:45], v[44:45], s[30:31]
	v_pk_add_f32 v[46:47], v[46:47], s[30:31]
	v_rcp_f32_e32 v40, v40
	v_pk_mul_f32 v[140:141], v[140:141], v[32:33]
	v_pk_mul_f32 v[142:143], v[142:143], v[34:35]
	v_rcp_f32_e32 v41, v41
	v_pk_mul_f32 v[156:157], v[156:157], v[36:37]
	v_pk_mul_f32 v[158:159], v[158:159], v[38:39]
	v_rcp_f32_e32 v42, v42
	v_cvt_pk_bf16_f32 v64, v140, v141
	v_cvt_pk_bf16_f32 v65, v142, v143
	v_rcp_f32_e32 v43, v43
	v_cvt_pk_bf16_f32 v66, v156, v157
	v_cvt_pk_bf16_f32 v67, v158, v159
	v_rcp_f32_e32 v44, v44
	global_store_dwordx2 v19, v[64:65], s[10:11]
	global_store_dwordx2 v19, v[66:67], s[10:11] offset:32
	v_rcp_f32_e32 v45, v45
	v_rcp_f32_e32 v46, v46
	v_rcp_f32_e32 v47, v47
	v_exp_f32_e32 v48, v48
	v_pk_mul_f32 v[236:237], v[236:237], v[26:27] op_sel_hi:[1,0]
	v_pk_mul_f32 v[238:239], v[238:239], v[26:27] op_sel_hi:[1,0]
	v_exp_f32_e32 v49, v49
	v_pk_mul_f32 v[252:253], v[252:253], v[26:27] op_sel_hi:[1,0]
	v_pk_mul_f32 v[254:255], v[254:255], v[26:27] op_sel_hi:[1,0]
	v_exp_f32_e32 v50, v50
	v_pk_mul_f32 v[32:33], v[236:237], s[26:27]
	v_pk_mul_f32 v[34:35], v[238:239], s[26:27]
	v_exp_f32_e32 v51, v51
	v_pk_mul_f32 v[36:37], v[252:253], s[26:27]
	v_pk_mul_f32 v[38:39], v[254:255], s[26:27]
	v_exp_f32_e32 v52, v52
	v_pk_fma_f32 v[32:33], v[236:237], v[32:33], s[28:29] neg_lo:[1,0,0] neg_hi:[1,0,0]
	v_pk_fma_f32 v[34:35], v[238:239], v[34:35], s[28:29] neg_lo:[1,0,0] neg_hi:[1,0,0]
	v_exp_f32_e32 v53, v53
	v_pk_fma_f32 v[36:37], v[252:253], v[36:37], s[28:29] neg_lo:[1,0,0] neg_hi:[1,0,0]
	v_pk_fma_f32 v[38:39], v[254:255], v[38:39], s[28:29] neg_lo:[1,0,0] neg_hi:[1,0,0]
	v_exp_f32_e32 v54, v54
	v_pk_mul_f32 v[32:33], v[236:237], v[32:33]
	v_pk_mul_f32 v[34:35], v[238:239], v[34:35]
	v_exp_f32_e32 v55, v55
	v_pk_mul_f32 v[36:37], v[252:253], v[36:37]
	v_pk_mul_f32 v[38:39], v[254:255], v[38:39]
	v_pk_add_f32 v[48:49], v[48:49], s[30:31]
	v_pk_add_f32 v[50:51], v[50:51], s[30:31]
	v_pk_add_f32 v[52:53], v[52:53], s[30:31]
	v_pk_add_f32 v[54:55], v[54:55], s[30:31]
	v_rcp_f32_e32 v48, v48
	v_pk_mul_f32 v[172:173], v[172:173], v[40:41]
	v_pk_mul_f32 v[174:175], v[174:175], v[42:43]
	v_rcp_f32_e32 v49, v49
	v_pk_mul_f32 v[188:189], v[188:189], v[44:45]
	v_pk_mul_f32 v[190:191], v[190:191], v[46:47]
	v_rcp_f32_e32 v50, v50
	v_cvt_pk_bf16_f32 v68, v172, v173
	v_cvt_pk_bf16_f32 v69, v174, v175
	v_rcp_f32_e32 v51, v51
	v_cvt_pk_bf16_f32 v70, v188, v189
	v_cvt_pk_bf16_f32 v71, v190, v191
	v_rcp_f32_e32 v52, v52
	global_store_dwordx2 v19, v[68:69], s[10:11] offset:64
	global_store_dwordx2 v19, v[70:71], s[10:11] offset:96
	v_rcp_f32_e32 v53, v53
	v_rcp_f32_e32 v54, v54
	v_rcp_f32_e32 v55, v55
	v_exp_f32_e32 v32, v32
	v_exp_f32_e32 v33, v33
	v_exp_f32_e32 v34, v34
	v_exp_f32_e32 v35, v35
	v_exp_f32_e32 v36, v36
	v_exp_f32_e32 v37, v37
	v_exp_f32_e32 v38, v38
	v_exp_f32_e32 v39, v39
	s_nop 0
	v_pk_add_f32 v[32:33], v[32:33], s[30:31]
	v_pk_add_f32 v[34:35], v[34:35], s[30:31]
	v_pk_add_f32 v[36:37], v[36:37], s[30:31]
	v_pk_add_f32 v[38:39], v[38:39], s[30:31]
	v_rcp_f32_e32 v32, v32
	v_pk_mul_f32 v[204:205], v[204:205], v[48:49]
	v_pk_mul_f32 v[206:207], v[206:207], v[50:51]
	v_rcp_f32_e32 v33, v33
	v_pk_mul_f32 v[220:221], v[220:221], v[52:53]
	v_pk_mul_f32 v[222:223], v[222:223], v[54:55]
	v_rcp_f32_e32 v34, v34
	v_cvt_pk_bf16_f32 v64, v204, v205
	v_cvt_pk_bf16_f32 v65, v206, v207
	v_rcp_f32_e32 v35, v35
	v_cvt_pk_bf16_f32 v66, v220, v221
	v_cvt_pk_bf16_f32 v67, v222, v223
	v_rcp_f32_e32 v36, v36
	global_store_dwordx2 v19, v[64:65], s[10:11] offset:128
	global_store_dwordx2 v19, v[66:67], s[10:11] offset:160
	v_rcp_f32_e32 v37, v37
	v_rcp_f32_e32 v38, v38
	v_rcp_f32_e32 v39, v39
	s_nop 0
	v_pk_mul_f32 v[236:237], v[236:237], v[32:33]
	v_pk_mul_f32 v[238:239], v[238:239], v[34:35]
	v_pk_mul_f32 v[252:253], v[252:253], v[36:37]
	v_pk_mul_f32 v[254:255], v[254:255], v[38:39]
	v_cvt_pk_bf16_f32 v68, v236, v237
	v_cvt_pk_bf16_f32 v69, v238, v239
	v_cvt_pk_bf16_f32 v70, v252, v253
	v_cvt_pk_bf16_f32 v71, v254, v255
	global_store_dwordx2 v19, v[68:69], s[10:11] offset:192
	global_store_dwordx2 v19, v[70:71], s[10:11] offset:224
